# P8 lru_pass1: next unit's conv-input row loads no longer drained right after issue; wait + clamp masks deferred until after the scan recurrence
# speedup vs baseline: 1.0015x; 1.0015x over previous
.LBB0_1303:
	s_and_b64 s[54:55], exec, s[54:55]
	s_cselect_b32 s54, 15, 1
	s_cselect_b32 s20, s67, 0x100
	s_and_b32 s54, s54, s56
	s_lshl_b32 s54, s54, 7
	v_or_b32_e32 v30, s54, v1
	s_add_i32 s60, s20, -1
	v_max_i32_e32 v2, 2, v30
	s_sub_u32 s54, s58, s54
	v_add_u32_e32 v2, -2, v2
	s_subb_u32 s55, s59, 0
	v_min_u32_e32 v154, s60, v2
	v_lshl_add_u64 v[2:3], s[54:55], 0, v[154:155]
	v_mov_b64_e32 v[26:27], s[6:7]
	s_mulk_i32 s56, 0xfb00
	s_add_i32 s57, s45, s35
	v_mad_u64_u32 v[4:5], s[58:59], v2, s78, v[26:27]
	s_add_i32 s56, s57, s56
	v_mov_b32_e32 v2, v5
	s_ashr_i32 s57, s56, 31
	v_mad_u64_u32 v[2:3], s[58:59], v3, s78, v[2:3]
	v_min_u32_e32 v10, s60, v30
	v_mov_b32_e32 v11, v155
	v_mov_b32_e32 v5, v2
	s_lshl_b64 s[56:57], s[56:57], 1
	v_or_b32_e32 v32, 2, v30
	v_lshl_add_u64 v[10:11], s[54:55], 0, v[10:11]
	v_lshl_add_u64 v[2:3], v[4:5], 0, s[56:57]
	v_max_i32_e32 v4, 1, v30
	v_mad_u64_u32 v[12:13], s[58:59], v10, s78, v[26:27]
	v_min_u32_e32 v18, s60, v32
	v_mov_b32_e32 v19, v155
	v_add_u32_e32 v4, -1, v4
	v_mov_b32_e32 v10, v13
	v_lshl_add_u64 v[18:19], s[54:55], 0, v[18:19]
	v_min_u32_e32 v4, s60, v4
	v_mov_b32_e32 v5, v155
	v_mad_u64_u32 v[10:11], s[58:59], v11, s78, v[10:11]
	v_mad_u64_u32 v[20:21], s[58:59], v18, s78, v[26:27]
	v_or_b32_e32 v31, 1, v30
	v_lshl_add_u64 v[4:5], s[54:55], 0, v[4:5]
	v_mov_b32_e32 v13, v10
	v_mov_b32_e32 v18, v21
	v_mad_u64_u32 v[6:7], s[58:59], v4, s78, v[26:27]
	v_lshl_add_u64 v[10:11], v[12:13], 0, s[56:57]
	v_min_u32_e32 v12, s60, v31
	v_mov_b32_e32 v13, v155
	v_mad_u64_u32 v[18:19], s[58:59], v19, s78, v[18:19]
	v_mov_b32_e32 v4, v7
	v_or_b32_e32 v33, 3, v30
	v_lshl_add_u64 v[12:13], s[54:55], 0, v[12:13]
	v_mov_b32_e32 v21, v18
	v_mad_u64_u32 v[4:5], s[58:59], v5, s78, v[4:5]
	v_mad_u64_u32 v[14:15], s[58:59], v12, s78, v[26:27]
	v_add_u32_e32 v34, 4, v30
	v_lshl_add_u64 v[18:19], v[20:21], 0, s[56:57]
	v_min_u32_e32 v20, s60, v33
	v_mov_b32_e32 v21, v155
	v_mov_b32_e32 v7, v4
	v_mov_b32_e32 v12, v15
	v_lshl_add_u64 v[20:21], s[54:55], 0, v[20:21]
	v_min_u32_e32 v28, s60, v34
	v_mov_b32_e32 v29, v155
	v_lshlrev_b32_e32 v154, 1, v158
	v_lshl_add_u64 v[4:5], v[6:7], 0, s[56:57]
	v_mad_u64_u32 v[12:13], s[58:59], v13, s78, v[12:13]
	v_mad_u64_u32 v[22:23], s[58:59], v20, s78, v[26:27]
	v_lshl_add_u64 v[28:29], s[54:55], 0, v[28:29]
	v_lshl_add_u64 v[2:3], v[2:3], 0, v[154:155]
	v_lshl_add_u64 v[6:7], v[4:5], 0, v[154:155]
	v_mov_b32_e32 v15, v12
	v_mov_b32_e32 v20, v23
	v_mad_u64_u32 v[26:27], s[54:55], v28, s78, v[26:27]
	global_load_dwordx4 v[38:41], v[2:3], off offset:2560
	s_nop 0
	global_load_dwordx4 v[42:45], v[6:7], off offset:2560
	v_lshl_add_u64 v[12:13], v[14:15], 0, s[56:57]
	v_mad_u64_u32 v[20:21], s[58:59], v21, s78, v[20:21]
	v_mov_b32_e32 v28, v27
	v_lshl_add_u64 v[10:11], v[10:11], 0, v[154:155]
	v_lshl_add_u64 v[14:15], v[12:13], 0, v[154:155]
	v_mov_b32_e32 v23, v20
	v_mad_u64_u32 v[28:29], s[54:55], v29, s78, v[28:29]
	global_load_dwordx4 v[46:49], v[10:11], off offset:2560
	s_nop 0
	global_load_dwordx4 v[50:53], v[14:15], off offset:2560
	v_lshl_add_u64 v[20:21], v[22:23], 0, s[56:57]
	v_mov_b32_e32 v27, v28
	v_lshl_add_u64 v[18:19], v[18:19], 0, v[154:155]
	v_lshl_add_u64 v[22:23], v[20:21], 0, v[154:155]
	v_lshl_add_u64 v[26:27], v[26:27], 0, s[56:57]
	global_load_dwordx4 v[54:57], v[18:19], off offset:2560
	s_nop 0
	global_load_dwordx4 v[58:61], v[22:23], off offset:2560
	v_lshl_add_u64 v[26:27], v[26:27], 0, v[154:155]
	global_load_dwordx4 v[62:65], v[26:27], off offset:2560
	v_mov_b32_e32 v66, v30
	s_mov_b32 s99, s20
.LBB0_1304:
	ds_read_b64 v[2:3], v238
	ds_read_b64 v[6:7], v237 offset:2016
	ds_read2_b64 v[14:17], v237 offset0:216 offset1:234
	v_or_b32_e32 v13, 64, v239
	v_or_b32_e32 v9, 0x80, v239
	s_waitcnt lgkmcnt(2)
	v_lshlrev_b32_e32 v4, 16, v2
	v_lshlrev_b32_e32 v8, 16, v3
	v_add_f32_e32 v10, 0, v4
	v_mul_f32_e32 v4, 0x3fb8aa3b, v4
	v_exp_f32_e32 v4, v4
	v_mul_f32_e32 v11, 0x3fb8aa3b, v8
	v_exp_f32_e32 v11, v11
	v_and_b32_e32 v2, 0xffff0000, v2
	v_fmac_f32_e32 v2, 0, v4
	v_and_b32_e32 v3, 0xffff0000, v3
	s_waitcnt lgkmcnt(1)
	v_lshlrev_b32_e32 v4, 16, v6
	v_add_f32_e32 v8, 0, v8
	v_fmac_f32_e32 v3, 0, v11
	v_lshlrev_b32_e32 v11, 16, v7
	v_add_f32_e32 v10, v10, v4
	v_mul_f32_e32 v4, 0x3fb8aa3b, v4
	v_add_f32_e32 v8, v8, v11
	v_exp_f32_e32 v4, v4
	v_mul_f32_e32 v11, 0x3fb8aa3b, v11
	v_exp_f32_e32 v11, v11
	v_and_b32_e32 v6, 0xffff0000, v6
	v_fmac_f32_e32 v6, v4, v2
	v_and_b32_e32 v2, 0xffff0000, v7
	v_fmac_f32_e32 v2, v11, v3
	s_waitcnt lgkmcnt(0)
	v_lshlrev_b32_e32 v3, 16, v16
	v_lshlrev_b32_e32 v4, 16, v17
	v_add_f32_e32 v7, v10, v3
	v_mul_f32_e32 v3, 0x3fb8aa3b, v3
	v_add_f32_e32 v8, v8, v4
	v_exp_f32_e32 v3, v3
	v_mul_f32_e32 v4, 0x3fb8aa3b, v4
	v_exp_f32_e32 v4, v4
	v_and_b32_e32 v10, 0xffff0000, v16
	v_fmac_f32_e32 v10, v3, v6
	v_and_b32_e32 v3, 0xffff0000, v17
	v_fmac_f32_e32 v3, v4, v2
	v_lshlrev_b32_e32 v2, 16, v14
	v_lshlrev_b32_e32 v4, 16, v15
	v_add_f32_e32 v6, v7, v2
	v_mul_f32_e32 v2, 0x3fb8aa3b, v2
	v_add_f32_e32 v7, v8, v4
	v_exp_f32_e32 v2, v2
	v_mul_f32_e32 v4, 0x3fb8aa3b, v4
	ds_read2_b64 v[16:19], v237 offset0:180 offset1:198
	v_exp_f32_e32 v4, v4
	v_and_b32_e32 v8, 0xffff0000, v14
	v_fmac_f32_e32 v8, v2, v10
	v_and_b32_e32 v2, 0xffff0000, v15
	v_fmac_f32_e32 v2, v4, v3
	s_waitcnt lgkmcnt(0)
	v_lshlrev_b32_e32 v3, 16, v18
	v_lshlrev_b32_e32 v4, 16, v19
	v_add_f32_e32 v6, v6, v3
	v_mul_f32_e32 v3, 0x3fb8aa3b, v3
	v_add_f32_e32 v7, v7, v4
	v_exp_f32_e32 v3, v3
	v_mul_f32_e32 v4, 0x3fb8aa3b, v4
	v_exp_f32_e32 v4, v4
	v_and_b32_e32 v10, 0xffff0000, v18
	v_fmac_f32_e32 v10, v3, v8
	v_and_b32_e32 v3, 0xffff0000, v19
	v_fmac_f32_e32 v3, v4, v2
	v_lshlrev_b32_e32 v2, 16, v16
	v_lshlrev_b32_e32 v4, 16, v17
	v_add_f32_e32 v6, v6, v2
	v_mul_f32_e32 v2, 0x3fb8aa3b, v2
	v_add_f32_e32 v7, v7, v4
	v_exp_f32_e32 v2, v2
	v_mul_f32_e32 v4, 0x3fb8aa3b, v4
	ds_read2_b64 v[18:21], v237 offset0:144 offset1:162
	v_exp_f32_e32 v4, v4
	v_and_b32_e32 v8, 0xffff0000, v16
	v_fmac_f32_e32 v8, v2, v10
	v_and_b32_e32 v2, 0xffff0000, v17
	v_fmac_f32_e32 v2, v4, v3
	s_waitcnt lgkmcnt(0)
	v_lshlrev_b32_e32 v3, 16, v20
	v_lshlrev_b32_e32 v4, 16, v21
	v_add_f32_e32 v6, v6, v3
	v_mul_f32_e32 v3, 0x3fb8aa3b, v3
	v_add_f32_e32 v7, v7, v4
	v_exp_f32_e32 v3, v3
	v_mul_f32_e32 v4, 0x3fb8aa3b, v4
	v_exp_f32_e32 v4, v4
	v_and_b32_e32 v10, 0xffff0000, v20
	v_fmac_f32_e32 v10, v3, v8
	v_and_b32_e32 v3, 0xffff0000, v21
	v_fmac_f32_e32 v3, v4, v2
	v_lshlrev_b32_e32 v2, 16, v18
	v_lshlrev_b32_e32 v4, 16, v19
	v_add_f32_e32 v6, v6, v2
	v_mul_f32_e32 v2, 0x3fb8aa3b, v2
	v_add_f32_e32 v7, v7, v4
	v_exp_f32_e32 v2, v2
	v_mul_f32_e32 v4, 0x3fb8aa3b, v4
	ds_read2_b64 v[14:17], v237 offset0:108 offset1:126
	v_exp_f32_e32 v4, v4
	v_and_b32_e32 v8, 0xffff0000, v18
	v_fmac_f32_e32 v8, v2, v10
	v_and_b32_e32 v2, 0xffff0000, v19
	v_fmac_f32_e32 v2, v4, v3
	s_waitcnt lgkmcnt(0)
	v_lshlrev_b32_e32 v3, 16, v16
	v_lshlrev_b32_e32 v4, 16, v17
	v_add_f32_e32 v6, v6, v3
	v_mul_f32_e32 v3, 0x3fb8aa3b, v3
	v_add_f32_e32 v7, v7, v4
	v_exp_f32_e32 v3, v3
	v_mul_f32_e32 v4, 0x3fb8aa3b, v4
	v_exp_f32_e32 v4, v4
	v_and_b32_e32 v10, 0xffff0000, v16
	v_fmac_f32_e32 v10, v3, v8
	v_and_b32_e32 v3, 0xffff0000, v17
	v_fmac_f32_e32 v3, v4, v2
	v_lshlrev_b32_e32 v2, 16, v14
	v_lshlrev_b32_e32 v4, 16, v15
	v_add_f32_e32 v6, v6, v2
	v_mul_f32_e32 v2, 0x3fb8aa3b, v2
	v_add_f32_e32 v7, v7, v4
	v_exp_f32_e32 v2, v2
	v_mul_f32_e32 v4, 0x3fb8aa3b, v4
	ds_read2_b64 v[16:19], v237 offset0:72 offset1:90
	v_exp_f32_e32 v4, v4
	v_and_b32_e32 v8, 0xffff0000, v14
	v_fmac_f32_e32 v8, v2, v10
	v_and_b32_e32 v2, 0xffff0000, v15
	v_fmac_f32_e32 v2, v4, v3
	s_waitcnt lgkmcnt(0)
	v_lshlrev_b32_e32 v3, 16, v18
	v_lshlrev_b32_e32 v4, 16, v19
	v_add_f32_e32 v6, v6, v3
	v_mul_f32_e32 v3, 0x3fb8aa3b, v3
	v_add_f32_e32 v7, v7, v4
	v_exp_f32_e32 v3, v3
	v_mul_f32_e32 v4, 0x3fb8aa3b, v4
	v_exp_f32_e32 v4, v4
	v_and_b32_e32 v10, 0xffff0000, v18
	v_fmac_f32_e32 v10, v3, v8
	v_and_b32_e32 v3, 0xffff0000, v19
	v_fmac_f32_e32 v3, v4, v2
	v_lshlrev_b32_e32 v2, 16, v16
	v_lshlrev_b32_e32 v4, 16, v17
	v_add_f32_e32 v6, v6, v2
	v_mul_f32_e32 v2, 0x3fb8aa3b, v2
	v_add_f32_e32 v7, v7, v4
	v_exp_f32_e32 v2, v2
	v_mul_f32_e32 v4, 0x3fb8aa3b, v4
	ds_read2_b64 v[18:21], v237 offset0:36 offset1:54
	v_exp_f32_e32 v4, v4
	v_and_b32_e32 v8, 0xffff0000, v16
	v_fmac_f32_e32 v8, v2, v10
	v_and_b32_e32 v2, 0xffff0000, v17
	v_fmac_f32_e32 v2, v4, v3
	s_waitcnt lgkmcnt(0)
	v_lshlrev_b32_e32 v3, 16, v20
	v_lshlrev_b32_e32 v4, 16, v21
	v_add_f32_e32 v6, v6, v3
	v_mul_f32_e32 v3, 0x3fb8aa3b, v3
	v_add_f32_e32 v7, v7, v4
	v_exp_f32_e32 v3, v3
	v_mul_f32_e32 v4, 0x3fb8aa3b, v4
	v_exp_f32_e32 v4, v4
	v_and_b32_e32 v10, 0xffff0000, v20
	v_fmac_f32_e32 v10, v3, v8
	v_and_b32_e32 v3, 0xffff0000, v21
	v_fmac_f32_e32 v3, v4, v2
	v_lshlrev_b32_e32 v2, 16, v18
	v_lshlrev_b32_e32 v4, 16, v19
	v_add_f32_e32 v6, v6, v2
	v_mul_f32_e32 v2, 0x3fb8aa3b, v2
	v_add_f32_e32 v7, v7, v4
	v_exp_f32_e32 v2, v2
	v_mul_f32_e32 v4, 0x3fb8aa3b, v4
	ds_read2_b64 v[14:17], v237 offset1:18
	v_exp_f32_e32 v4, v4
	v_and_b32_e32 v8, 0xffff0000, v18
	v_fmac_f32_e32 v8, v2, v10
	v_and_b32_e32 v2, 0xffff0000, v19
	v_fmac_f32_e32 v2, v4, v3
	s_waitcnt lgkmcnt(0)
	v_lshlrev_b32_e32 v3, 16, v16
	v_lshlrev_b32_e32 v4, 16, v17
	v_add_f32_e32 v6, v6, v3
	v_mul_f32_e32 v3, 0x3fb8aa3b, v3
	v_add_f32_e32 v7, v7, v4
	v_exp_f32_e32 v3, v3
	v_mul_f32_e32 v4, 0x3fb8aa3b, v4
	v_exp_f32_e32 v4, v4
	v_and_b32_e32 v10, 0xffff0000, v16
	v_fmac_f32_e32 v10, v3, v8
	v_and_b32_e32 v3, 0xffff0000, v17
	v_fmac_f32_e32 v3, v4, v2
	v_lshlrev_b32_e32 v2, 16, v14
	v_lshlrev_b32_e32 v4, 16, v15
	v_mul_f32_e32 v8, 0x3fb8aa3b, v2
	v_add_f32_e32 v2, v6, v2
	v_add_f32_e32 v6, v7, v4
	v_mul_f32_e32 v4, 0x3fb8aa3b, v4
	v_mul_f32_e32 v2, 0x3fb8aa3b, v2
	v_exp_f32_e32 v8, v8
	v_and_b32_e32 v16, 0xffff0000, v14
	v_exp_f32_e32 v4, v4
	v_exp_f32_e32 v14, v2
	v_mul_f32_e32 v2, 0x3fb8aa3b, v6
	v_exp_f32_e32 v17, v2
	v_and_b32_e32 v18, 0xffff0000, v15
	v_or_b32_e32 v5, 0xc0, v239
	v_fmac_f32_e32 v16, v8, v10
	v_fmac_f32_e32 v18, v4, v3
	ds_bpermute_b32 v2, v5, v14
	ds_bpermute_b32 v3, v5, v17
	ds_bpermute_b32 v4, v5, v16
	ds_bpermute_b32 v5, v5, v18
	ds_bpermute_b32 v6, v9, v14
	ds_bpermute_b32 v7, v9, v17
	ds_bpermute_b32 v8, v9, v16
	ds_bpermute_b32 v9, v9, v18
	ds_bpermute_b32 v10, v13, v14
	ds_bpermute_b32 v11, v13, v17
	ds_bpermute_b32 v12, v13, v16
	ds_bpermute_b32 v13, v13, v18
	ds_bpermute_b32 v14, v239, v14
	ds_bpermute_b32 v15, v239, v17
	ds_bpermute_b32 v16, v239, v16
	ds_bpermute_b32 v17, v239, v18
	s_and_b64 vcc, exec, s[52:53]
	s_cbranch_vccnz .Lp8_nomask
	s_waitcnt vmcnt(0)
	v_add_u32_e32 v67, -1, v66
	v_cmp_gt_u32_e32 vcc, s99, v67
	s_nop 1
	v_cndmask_b32_e32 v201, 0, v38, vcc
	v_cndmask_b32_e32 v202, 0, v39, vcc
	v_cndmask_b32_e32 v203, 0, v40, vcc
	v_cndmask_b32_e32 v205, 0, v41, vcc
	v_cndmask_b32_e32 v206, 0, v42, vcc
	v_cndmask_b32_e32 v207, 0, v43, vcc
	v_cndmask_b32_e32 v209, 0, v44, vcc
	v_cndmask_b32_e32 v210, 0, v45, vcc
	v_cmp_gt_u32_e32 vcc, s99, v66
	s_nop 1
	v_cndmask_b32_e32 v212, 0, v46, vcc
	v_cndmask_b32_e32 v213, 0, v47, vcc
	v_cndmask_b32_e32 v215, 0, v48, vcc
	v_cndmask_b32_e32 v216, 0, v49, vcc
	v_or_b32_e32 v67, 1, v66
	v_cmp_gt_u32_e32 vcc, s99, v67
	s_nop 1
	v_cndmask_b32_e32 v218, 0, v50, vcc
	v_cndmask_b32_e32 v219, 0, v51, vcc
	v_cndmask_b32_e32 v221, 0, v52, vcc
	v_cndmask_b32_e32 v222, 0, v53, vcc
	v_or_b32_e32 v67, 2, v66
	v_cmp_gt_u32_e32 vcc, s99, v67
	s_nop 1
	v_cndmask_b32_e32 v224, 0, v54, vcc
	v_cndmask_b32_e32 v225, 0, v55, vcc
	v_cndmask_b32_e32 v226, 0, v56, vcc
	v_cndmask_b32_e32 v227, 0, v57, vcc
	v_or_b32_e32 v67, 3, v66
	v_cmp_gt_u32_e32 vcc, s99, v67
	s_nop 1
	v_cndmask_b32_e32 v228, 0, v58, vcc
	v_cndmask_b32_e32 v229, 0, v59, vcc
	v_cndmask_b32_e32 v230, 0, v60, vcc
	v_cndmask_b32_e32 v231, 0, v61, vcc
	v_add_u32_e32 v67, 4, v66
	v_cmp_gt_u32_e32 vcc, s99, v67
	s_nop 1
	v_cndmask_b32_e32 v232, 0, v62, vcc
	v_cndmask_b32_e32 v233, 0, v63, vcc
	v_cndmask_b32_e32 v234, 0, v64, vcc
	v_cndmask_b32_e32 v235, 0, v65, vcc
.Lp8_nomask:
	s_and_saveexec_b64 s[54:55], s[0:1]
	s_cbranch_execz .LBB0_1306
	s_waitcnt lgkmcnt(10)
	v_pk_mul_f32 v[18:19], v[2:3], v[6:7]
	v_pk_fma_f32 v[2:3], v[2:3], 0, v[4:5] op_sel_hi:[1,0,1]
	v_mad_i64_i32 v[4:5], s[56:57], s81, v240, v[94:95]
	s_waitcnt lgkmcnt(8)
	v_pk_fma_f32 v[2:3], v[2:3], v[6:7], v[8:9]
	s_waitcnt lgkmcnt(6)
	v_pk_mul_f32 v[18:19], v[18:19], v[10:11]
	s_waitcnt lgkmcnt(4)
	v_pk_fma_f32 v[2:3], v[2:3], v[10:11], v[12:13]
	v_lshl_add_u64 v[4:5], v[4:5], 2, v[166:167]
	s_waitcnt lgkmcnt(2)
	v_pk_mul_f32 v[18:19], v[18:19], v[14:15]
	s_waitcnt lgkmcnt(0)
	v_pk_fma_f32 v[2:3], v[2:3], v[14:15], v[16:17]
	v_lshl_add_u64 v[6:7], s[8:9], 0, v[4:5]
	v_lshl_add_u64 v[4:5], s[10:11], 0, v[4:5]
	global_store_dwordx2 v[6:7], v[18:19], off
	global_store_dwordx2 v[4:5], v[2:3], off
